# routing logits loop software-pipelined: next k-step's 16 fragment loads requested before the current step's MFMAs (shadow registers)
# baseline (speedup 1.0000x reference)
; template <int MODE, bool OUTF32, bool HIN16 = false, bool HOUT16 = false>
; __device__ __forceinline__ void row_phase(LAS unsigned char* lds, const RowArgs& a, int G) {
;     ...
;         if (MODE == RM_ROUTE && tid < 32) cntl[tid] = 0;
;         f32x4 xs[RG];
;         if constexpr (MODE == RM_ROUTE && HIN16) {
;             const int fr = lane & 15, fq = lane >> 4;
;             f32x4 acc[2][3]; float sq[2] = {0.f, 0.f};
; #pragma unroll
;             for (int mt = 0; mt < 2; ++mt)
; #pragma unroll
;                 for (int nt = 0; nt < 3; ++nt) acc[mt][nt] = (f32x4){0.f, 0.f, 0.f, 0.f};
; #pragma unroll 2
;             for (int ks = 0; ks < 8; ++ks) { const int k0 = 256 * wave + 32 * ks + 8 * fq;
;                 bf16x8 af[2], bh[3], bl[3];
; #pragma unroll
;                 for (int mt = 0; mt < 2; ++mt) af[mt] = *(const bf16x8*)(a.hin16 + (size_t)(row0 + 16 * mt + fr) * D + k0);
; #pragma unroll
;                 for (int nt = 0; nt < 3; ++nt) { bh[nt] = *(const bf16x8*)(a.wr + (size_t)(16 * nt + fr) * D + k0); bl[nt] = *(const bf16x8*)(a.wr + (size_t)(48 + 16 * nt + fr) * D + k0); }
.LBB0_1107:
	s_and_saveexec_b64 s[12:13], s[2:3]
	ds_write_b32 v50, v5 offset:46208
	s_or_b64 exec, exec, s[12:13]
	s_lshl_b32 s63, s53, 5
	v_or_b32_e32 v2, s63, v51
	v_ashrrev_i32_e32 v3, 31, v2
	v_lshlrev_b64 v[42:43], 12, v[2:3]
	v_or_b32_e32 v2, 16, v2
	v_ashrrev_i32_e32 v3, 31, v2
	v_lshlrev_b64 v[44:45], 12, v[2:3]
	v_mov_b32_e32 v14, 0
	v_lshl_add_u64 v[46:47], s[34:35], 0, v[42:43]
	v_lshl_add_u64 v[48:49], s[34:35], 0, v[44:45]
	s_mov_b32 s12, 0
	v_mov_b32_e32 v15, v14
	v_mov_b32_e32 v16, v14
	v_mov_b32_e32 v17, v14
	v_mov_b32_e32 v22, v14
	v_mov_b32_e32 v23, v14
	v_mov_b32_e32 v24, v14
	v_mov_b32_e32 v25, v14
	v_mov_b32_e32 v26, v14
	v_mov_b32_e32 v27, v14
	v_mov_b32_e32 v28, v14
	v_mov_b32_e32 v29, v14
	v_mov_b32_e32 v10, v14
	v_mov_b32_e32 v11, v14
	v_mov_b32_e32 v12, v14
	v_mov_b32_e32 v13, v14
	v_mov_b32_e32 v18, v14
	v_mov_b32_e32 v19, v14
	v_mov_b32_e32 v20, v14
	v_mov_b32_e32 v21, v14
	v_mov_b32_e32 v6, v14
	v_mov_b32_e32 v7, v14
	v_mov_b32_e32 v8, v14
	v_mov_b32_e32 v9, v14
	v_mov_b32_e32 v2, v14
	v_mov_b32_e32 v3, v14
	s_mov_b32 s98, 0
	v_add_u32_e32 v158, s98, v60
	v_ashrrev_i32_e32 v159, 31, v158
	v_add_u32_e32 v160, 32, v158
	v_lshlrev_b64 v[158:159], 1, v[158:159]
	v_lshl_add_u64 v[162:163], s[34:35], 0, v[158:159]
	v_lshl_add_u64 v[158:159], s[46:47], 0, v[158:159]
	v_lshl_add_u64 v[174:175], v[158:159], 0, v[36:37]
	v_add_co_u32_e32 v194, vcc, s54, v174
	v_ashrrev_i32_e32 v161, 31, v160
	s_nop 0
	v_addc_co_u32_e32 v195, vcc, 0, v175, vcc
	v_add_co_u32_e32 v198, vcc, s55, v174
	v_lshlrev_b64 v[160:161], 1, v[160:161]
	s_nop 0
	v_addc_co_u32_e32 v199, vcc, 0, v175, vcc
	v_add_co_u32_e32 v192, vcc, s56, v174
	v_lshl_add_u64 v[164:165], v[162:163], 0, v[42:43]
	v_lshl_add_u64 v[162:163], v[162:163], 0, v[44:45]
	v_addc_co_u32_e32 v193, vcc, 0, v175, vcc
	v_lshl_add_u64 v[170:171], v[158:159], 0, v[38:39]
	v_lshl_add_u64 v[176:177], v[46:47], 0, v[160:161]
	v_lshl_add_u64 v[178:179], v[48:49], 0, v[160:161]
	v_lshl_add_u64 v[190:191], v[32:33], 0, v[160:161]
	v_lshl_add_u64 v[186:187], v[34:35], 0, v[160:161]
	global_load_dwordx4 v[158:161], v[164:165], off
	s_nop 0
	global_load_dwordx4 v[162:165], v[162:163], off
	s_nop 0
	global_load_dwordx4 v[166:169], v[174:175], off
	v_add_co_u32_e32 v202, vcc, s57, v174
	global_load_dwordx4 v[170:173], v[170:171], off
	s_nop 0
	v_addc_co_u32_e32 v203, vcc, 0, v175, vcc
	v_add_co_u32_e32 v210, vcc, s54, v190
	global_load_dwordx4 v[174:177], v[176:177], off
	s_nop 0
	global_load_dwordx4 v[178:181], v[178:179], off
	s_nop 0
	global_load_dwordx4 v[182:185], v[190:191], off
	v_addc_co_u32_e32 v211, vcc, 0, v191, vcc
	v_add_co_u32_e32 v214, vcc, s55, v190
	global_load_dwordx4 v[186:189], v[186:187], off
	s_nop 0
	v_addc_co_u32_e32 v215, vcc, 0, v191, vcc
	v_add_co_u32_e32 v206, vcc, s56, v190
	s_nop 0
	s_nop 0
	v_addc_co_u32_e32 v207, vcc, 0, v191, vcc
	v_add_co_u32_e32 v218, vcc, s57, v190
	s_nop 0
	s_nop 0
	v_addc_co_u32_e32 v219, vcc, 0, v191, vcc
	global_load_dwordx4 v[190:193], v[192:193], off
	s_nop 0
	global_load_dwordx4 v[194:197], v[194:195], off
	s_nop 0
	global_load_dwordx4 v[198:201], v[198:199], off
	s_nop 0
	global_load_dwordx4 v[202:205], v[202:203], off
	s_nop 0
	global_load_dwordx4 v[206:209], v[206:207], off
	s_nop 0
	global_load_dwordx4 v[210:213], v[210:211], off
	s_nop 0
	global_load_dwordx4 v[214:217], v[214:215], off
	s_nop 0
	global_load_dwordx4 v[218:221], v[218:219], off
	s_waitcnt vmcnt(0)
	v_mov_b32_e32 v66, v158
	v_mov_b32_e32 v67, v159
	v_mov_b32_e32 v68, v160
	v_mov_b32_e32 v69, v161
	v_mov_b32_e32 v70, v162
	v_mov_b32_e32 v71, v163
	v_mov_b32_e32 v72, v164
	v_mov_b32_e32 v73, v165
	v_mov_b32_e32 v74, v166
	v_mov_b32_e32 v75, v167
	v_mov_b32_e32 v76, v168
	v_mov_b32_e32 v77, v169
	v_mov_b32_e32 v78, v170
	v_mov_b32_e32 v79, v171
	v_mov_b32_e32 v80, v172
	v_mov_b32_e32 v81, v173
	v_mov_b32_e32 v82, v174
	v_mov_b32_e32 v83, v175
	v_mov_b32_e32 v84, v176
	v_mov_b32_e32 v85, v177
	v_mov_b32_e32 v86, v178
	v_mov_b32_e32 v87, v179
	v_mov_b32_e32 v88, v180
	v_mov_b32_e32 v89, v181
	v_mov_b32_e32 v90, v182
	v_mov_b32_e32 v91, v183
	v_mov_b32_e32 v92, v184
	v_mov_b32_e32 v93, v185
	v_mov_b32_e32 v94, v186
	v_mov_b32_e32 v95, v187
	v_mov_b32_e32 v96, v188
	v_mov_b32_e32 v97, v189
	v_mov_b32_e32 v98, v190
	v_mov_b32_e32 v99, v191
	v_mov_b32_e32 v100, v192
	v_mov_b32_e32 v101, v193
	v_mov_b32_e32 v102, v194
	v_mov_b32_e32 v103, v195
	v_mov_b32_e32 v104, v196
	v_mov_b32_e32 v105, v197
	v_mov_b32_e32 v106, v198
	v_mov_b32_e32 v107, v199
	v_mov_b32_e32 v108, v200
	v_mov_b32_e32 v109, v201
	v_mov_b32_e32 v110, v202
	v_mov_b32_e32 v111, v203
	v_mov_b32_e32 v112, v204
	v_mov_b32_e32 v113, v205
	v_mov_b32_e32 v114, v206
	v_mov_b32_e32 v115, v207
	v_mov_b32_e32 v116, v208
	v_mov_b32_e32 v117, v209
	v_mov_b32_e32 v118, v210
	v_mov_b32_e32 v119, v211
	v_mov_b32_e32 v120, v212
	v_mov_b32_e32 v121, v213
	v_mov_b32_e32 v122, v214
	v_mov_b32_e32 v123, v215
	v_mov_b32_e32 v124, v216
	v_mov_b32_e32 v125, v217
	v_mov_b32_e32 v126, v218
	v_mov_b32_e32 v127, v219
	v_mov_b32_e32 v128, v220
	v_mov_b32_e32 v129, v221
; #define MFMA16(b, a, c) __builtin_amdgcn_mfma_f32_16x16x32_bf16((b), (a), (c), 0, 0, 0)
; template <int MODE, bool OUTF32, bool HIN16 = false, bool HOUT16 = false>
; __device__ __forceinline__ void row_phase(LAS unsigned char* lds, const RowArgs& a, int G) {
;     ...
;             for (int ks = 0; ks < 8; ++ks) { const int k0 = 256 * wave + 32 * ks + 8 * fq;
;                 bf16x8 af[2], bh[3], bl[3];
; #pragma unroll
;                 for (int mt = 0; mt < 2; ++mt) af[mt] = *(const bf16x8*)(a.hin16 + (size_t)(row0 + 16 * mt + fr) * D + k0);
; #pragma unroll
;                 for (int nt = 0; nt < 3; ++nt) { bh[nt] = *(const bf16x8*)(a.wr + (size_t)(16 * nt + fr) * D + k0); bl[nt] = *(const bf16x8*)(a.wr + (size_t)(48 + 16 * nt + fr) * D + k0); }
; #pragma unroll
;                 for (int mt = 0; mt < 2; ++mt) {
; #pragma unroll
;                     for (int e = 0; e < 8; ++e) { const float v = bf2f((unsigned short)af[mt][e]); sq[mt] += v * v; }
; #pragma unroll
;                     for (int nt = 0; nt < 3; ++nt) { acc[mt][nt] = MFMA16(bh[nt], af[mt], acc[mt][nt]); acc[mt][nt] = MFMA16(bl[nt], af[mt], acc[mt][nt]); } }
.LBB0_1110:
	s_add_i32 s98, s12, 64
	s_min_u32 s98, s98, 0xc0
	v_add_u32_e32 v158, s98, v60
	v_ashrrev_i32_e32 v159, 31, v158
	v_add_u32_e32 v160, 32, v158
	v_lshlrev_b64 v[158:159], 1, v[158:159]
	v_lshl_add_u64 v[162:163], s[34:35], 0, v[158:159]
	v_lshl_add_u64 v[158:159], s[46:47], 0, v[158:159]
	v_lshl_add_u64 v[174:175], v[158:159], 0, v[36:37]
	v_add_co_u32_e32 v194, vcc, s54, v174
	v_ashrrev_i32_e32 v161, 31, v160
	s_nop 0
	v_addc_co_u32_e32 v195, vcc, 0, v175, vcc
	v_add_co_u32_e32 v198, vcc, s55, v174
	v_lshlrev_b64 v[160:161], 1, v[160:161]
	s_nop 0
	v_addc_co_u32_e32 v199, vcc, 0, v175, vcc
	v_add_co_u32_e32 v192, vcc, s56, v174
	v_lshl_add_u64 v[164:165], v[162:163], 0, v[42:43]
	v_lshl_add_u64 v[162:163], v[162:163], 0, v[44:45]
	v_addc_co_u32_e32 v193, vcc, 0, v175, vcc
	v_lshl_add_u64 v[170:171], v[158:159], 0, v[38:39]
	v_lshl_add_u64 v[176:177], v[46:47], 0, v[160:161]
	v_lshl_add_u64 v[178:179], v[48:49], 0, v[160:161]
	v_lshl_add_u64 v[190:191], v[32:33], 0, v[160:161]
	v_lshl_add_u64 v[186:187], v[34:35], 0, v[160:161]
	global_load_dwordx4 v[158:161], v[164:165], off
	s_nop 0
	global_load_dwordx4 v[162:165], v[162:163], off
	s_nop 0
	global_load_dwordx4 v[166:169], v[174:175], off
	v_add_co_u32_e32 v202, vcc, s57, v174
	global_load_dwordx4 v[170:173], v[170:171], off
	s_nop 0
	v_addc_co_u32_e32 v203, vcc, 0, v175, vcc
	v_add_co_u32_e32 v210, vcc, s54, v190
	global_load_dwordx4 v[174:177], v[176:177], off
	s_nop 0
	global_load_dwordx4 v[178:181], v[178:179], off
	s_nop 0
	global_load_dwordx4 v[182:185], v[190:191], off
	v_addc_co_u32_e32 v211, vcc, 0, v191, vcc
	v_add_co_u32_e32 v214, vcc, s55, v190
	global_load_dwordx4 v[186:189], v[186:187], off
	s_nop 0
	v_addc_co_u32_e32 v215, vcc, 0, v191, vcc
	v_add_co_u32_e32 v206, vcc, s56, v190
	s_nop 0
	s_nop 0
	v_addc_co_u32_e32 v207, vcc, 0, v191, vcc
	v_add_co_u32_e32 v218, vcc, s57, v190
	s_nop 0
	s_nop 0
	v_addc_co_u32_e32 v219, vcc, 0, v191, vcc
	global_load_dwordx4 v[190:193], v[192:193], off
	s_nop 0
	global_load_dwordx4 v[194:197], v[194:195], off
	s_nop 0
	global_load_dwordx4 v[198:201], v[198:199], off
	s_nop 0
	global_load_dwordx4 v[202:205], v[202:203], off
	s_nop 0
	global_load_dwordx4 v[206:209], v[206:207], off
	s_nop 0
	global_load_dwordx4 v[210:213], v[210:211], off
	s_nop 0
	global_load_dwordx4 v[214:217], v[214:215], off
	s_nop 0
	global_load_dwordx4 v[218:221], v[218:219], off
	v_mfma_f32_16x16x32_bf16 v[26:29], v[74:77], v[66:69], v[26:29]
	v_and_b32_e32 v131, 0xffff0000, v70
	v_lshlrev_b32_e32 v130, 16, v70
	v_lshlrev_b32_e32 v4, 16, v66
	v_mfma_f32_16x16x32_bf16 v[10:13], v[74:77], v[70:73], v[10:13]
	v_and_b32_e32 v40, 0xffff0000, v66
	v_and_b32_e32 v133, 0xffff0000, v71
	v_lshlrev_b32_e32 v132, 16, v71
	v_mfma_f32_16x16x32_bf16 v[26:29], v[102:105], v[66:69], v[26:29]
	v_lshlrev_b32_e32 v65, 16, v67
	v_and_b32_e32 v139, 0xffff0000, v67
	v_lshlrev_b32_e32 v141, 16, v68
	v_mfma_f32_16x16x32_bf16 v[10:13], v[102:105], v[70:73], v[10:13]
	v_mul_f32_e64 v102, v130, v130
	v_mul_f32_e64 v103, v131, v131
	v_pk_mul_f32 v[104:105], v[132:133], v[132:133]
	v_and_b32_e32 v135, 0xffff0000, v72
	v_mfma_f32_16x16x32_bf16 v[14:17], v[98:101], v[66:69], v[14:17]
	v_lshlrev_b32_e32 v134, 16, v72
	v_mul_f32_e32 v138, v65, v65
	v_mul_f32_e32 v140, v139, v139
	v_mfma_f32_16x16x32_bf16 v[6:9], v[98:101], v[70:73], v[6:9]
	v_mul_f32_e32 v98, v4, v4
	v_mov_b32_e32 v99, v102
	v_mul_f32_e32 v100, v40, v40
	v_mfma_f32_16x16x32_bf16 v[22:25], v[78:81], v[66:69], v[22:25]
	v_mov_b32_e32 v101, v103
	v_pk_add_f32 v[2:3], v[2:3], v[98:99]
	v_mov_b32_e32 v139, v104
	v_mfma_f32_16x16x32_bf16 v[18:21], v[78:81], v[70:73], v[18:21]
	v_add_f32_e64 v2, v100, v2
	v_add_f32_e64 v3, v101, v3
	v_and_b32_e32 v143, 0xffff0000, v68
	v_mul_f32_e32 v142, v141, v141
	v_pk_mul_f32 v[130:131], v[134:135], v[134:135]
	v_mov_b32_e32 v141, v105
	v_pk_add_f32 v[2:3], v[138:139], v[2:3]
	v_lshlrev_b32_e32 v145, 16, v69
	v_and_b32_e32 v137, 0xffff0000, v73
	v_lshlrev_b32_e32 v136, 16, v73
	v_mul_f32_e32 v144, v143, v143
	v_mov_b32_e32 v143, v130
	v_pk_add_f32 v[2:3], v[140:141], v[2:3]
	v_and_b32_e32 v147, 0xffff0000, v69
	v_mfma_f32_16x16x32_bf16 v[22:25], v[106:109], v[66:69], v[22:25]
	v_mul_f32_e32 v146, v145, v145
	v_mov_b32_e32 v145, v131
	v_pk_add_f32 v[2:3], v[142:143], v[2:3]
	v_mfma_f32_16x16x32_bf16 v[18:21], v[106:109], v[70:73], v[18:21]
	v_mul_f32_e64 v106, v136, v136
	v_mul_f32_e64 v107, v137, v137
	v_lshlrev_b32_e32 v149, 16, v82
	v_and_b32_e32 v75, 0xffff0000, v86
	v_mfma_f32_16x16x32_bf16 v[14:17], v[110:113], v[66:69], v[14:17]
	v_lshlrev_b32_e32 v74, 16, v86
; #define MFMA16(b, a, c) __builtin_amdgcn_mfma_f32_16x16x32_bf16((b), (a), (c), 0, 0, 0)
; template <int MODE, bool OUTF32, bool HIN16 = false, bool HOUT16 = false>
; __device__ __forceinline__ void row_phase(LAS unsigned char* lds, const RowArgs& a, int G) {
;     ...
;                 for (int mt = 0; mt < 2; ++mt) {
; #pragma unroll
;                     for (int e = 0; e < 8; ++e) { const float v = bf2f((unsigned short)af[mt][e]); sq[mt] += v * v; }
; #pragma unroll
;                     for (int nt = 0; nt < 3; ++nt) { acc[mt][nt] = MFMA16(bh[nt], af[mt], acc[mt][nt]); acc[mt][nt] = MFMA16(bl[nt], af[mt], acc[mt][nt]); } }
;             }
; #pragma unroll
;             for (int mt = 0; mt < 2; ++mt) { const int r = 16 * mt + fr;
; #pragma unroll
;                 for (int nt = 0; nt < 3; ++nt)
; #pragma unroll
;                     for (int i = 0; i < 4; ++i) { const int o = 16 * nt + 4 * fq + i; if (o < 36) red[(r * 8 + wave) * NRED + o] = acc[mt][nt][i]; }
;                 float s = sq[mt]; s += __shfl_xor(s, 16); s += __shfl_xor(s, 32);
;                 if (fq == 0) red[(r * 8 + wave) * NRED + 36] = s; }
	v_mul_f32_e32 v148, v147, v147
	v_mov_b32_e32 v147, v106
	v_mfma_f32_16x16x32_bf16 v[6:9], v[110:113], v[70:73], v[6:9]
	v_add_f32_e64 v2, v144, v2
	v_add_f32_e64 v3, v145, v3
	v_mul_f32_e32 v108, v149, v149
	v_pk_mul_f32 v[74:75], v[74:75], v[74:75]
	v_mov_b32_e32 v149, v107
	v_pk_add_f32 v[2:3], v[146:147], v[2:3]
	v_and_b32_e32 v150, 0xffff0000, v82
	v_and_b32_e32 v77, 0xffff0000, v87
	v_lshlrev_b32_e32 v76, 16, v87
	v_mov_b32_e32 v109, v74
	v_pk_add_f32 v[2:3], v[148:149], v[2:3]
	v_lshlrev_b32_e32 v151, 16, v83
	v_mul_f32_e32 v132, v150, v150
	v_mfma_f32_16x16x32_bf16 v[26:29], v[90:93], v[82:85], v[26:29]
	v_mul_f32_e64 v76, v76, v76
	v_mul_f32_e64 v77, v77, v77
	v_mov_b32_e32 v133, v75
	v_pk_add_f32 v[2:3], v[2:3], v[108:109]
	v_mfma_f32_16x16x32_bf16 v[22:25], v[94:97], v[82:85], v[22:25]
	v_and_b32_e32 v152, 0xffff0000, v83
	v_and_b32_e32 v79, 0xffff0000, v88
	v_lshlrev_b32_e32 v78, 16, v88
	v_mfma_f32_16x16x32_bf16 v[10:13], v[90:93], v[86:89], v[10:13]
	v_mul_f32_e32 v66, v151, v151
	v_mov_b32_e32 v67, v76
	v_pk_add_f32 v[2:3], v[132:133], v[2:3]
	v_mfma_f32_16x16x32_bf16 v[18:21], v[94:97], v[86:89], v[18:21]
	v_lshlrev_b32_e32 v153, 16, v84
	v_mul_f32_e32 v68, v152, v152
	v_pk_mul_f32 v[78:79], v[78:79], v[78:79]
	v_mfma_f32_16x16x32_bf16 v[14:17], v[114:117], v[82:85], v[14:17]
	v_mov_b32_e32 v69, v77
	v_pk_add_f32 v[2:3], v[66:67], v[2:3]
	v_and_b32_e32 v154, 0xffff0000, v84
	v_mfma_f32_16x16x32_bf16 v[6:9], v[114:117], v[86:89], v[6:9]
	v_and_b32_e32 v81, 0xffff0000, v89
	v_lshlrev_b32_e32 v80, 16, v89
	v_mul_f32_e32 v134, v153, v153
	v_mov_b32_e32 v135, v78
	v_pk_add_f32 v[2:3], v[68:69], v[2:3]
	v_lshlrev_b32_e32 v155, 16, v85
	v_mul_f32_e32 v70, v154, v154
	v_pk_mul_f32 v[80:81], v[80:81], v[80:81]
	v_mov_b32_e32 v71, v79
	v_mfma_f32_16x16x32_bf16 v[26:29], v[118:121], v[82:85], v[26:29]
	v_add_f32_e64 v2, v134, v2
	v_add_f32_e64 v3, v135, v3
	v_and_b32_e32 v156, 0xffff0000, v85
	v_mul_f32_e32 v72, v155, v155
	v_mfma_f32_16x16x32_bf16 v[22:25], v[122:125], v[82:85], v[22:25]
	v_mov_b32_e32 v73, v80
	v_pk_add_f32 v[2:3], v[70:71], v[2:3]
	v_mul_f32_e32 v110, v156, v156
	v_mfma_f32_16x16x32_bf16 v[10:13], v[118:121], v[86:89], v[10:13]
	v_mov_b32_e32 v111, v81
	v_pk_add_f32 v[2:3], v[72:73], v[2:3]
	v_mfma_f32_16x16x32_bf16 v[18:21], v[122:125], v[86:89], v[18:21]
	v_add_f32_e64 v2, v110, v2
	v_add_f32_e64 v3, v111, v3
	v_mfma_f32_16x16x32_bf16 v[14:17], v[126:129], v[82:85], v[14:17]
	v_mfma_f32_16x16x32_bf16 v[6:9], v[126:129], v[86:89], v[6:9]
	s_waitcnt vmcnt(0)
	v_mov_b32_e32 v66, v158
	v_mov_b32_e32 v67, v159
	v_mov_b32_e32 v68, v160
	v_mov_b32_e32 v69, v161
	v_mov_b32_e32 v70, v162
	v_mov_b32_e32 v71, v163
	v_mov_b32_e32 v72, v164
	v_mov_b32_e32 v73, v165
	v_mov_b32_e32 v74, v166
	v_mov_b32_e32 v75, v167
	v_mov_b32_e32 v76, v168
	v_mov_b32_e32 v77, v169
	v_mov_b32_e32 v78, v170
	v_mov_b32_e32 v79, v171
	v_mov_b32_e32 v80, v172
	v_mov_b32_e32 v81, v173
	v_mov_b32_e32 v82, v174
	v_mov_b32_e32 v83, v175
	v_mov_b32_e32 v84, v176
	v_mov_b32_e32 v85, v177
	v_mov_b32_e32 v86, v178
	v_mov_b32_e32 v87, v179
	v_mov_b32_e32 v88, v180
	v_mov_b32_e32 v89, v181
	v_mov_b32_e32 v90, v182
	v_mov_b32_e32 v91, v183
	v_mov_b32_e32 v92, v184
	v_mov_b32_e32 v93, v185
	v_mov_b32_e32 v94, v186
	v_mov_b32_e32 v95, v187
	v_mov_b32_e32 v96, v188
	v_mov_b32_e32 v97, v189
	v_mov_b32_e32 v98, v190
	v_mov_b32_e32 v99, v191
	v_mov_b32_e32 v100, v192
	v_mov_b32_e32 v101, v193
	v_mov_b32_e32 v102, v194
	v_mov_b32_e32 v103, v195
	v_mov_b32_e32 v104, v196
	v_mov_b32_e32 v105, v197
	v_mov_b32_e32 v106, v198
	v_mov_b32_e32 v107, v199
	v_mov_b32_e32 v108, v200
	v_mov_b32_e32 v109, v201
	v_mov_b32_e32 v110, v202
	v_mov_b32_e32 v111, v203
	v_mov_b32_e32 v112, v204
	v_mov_b32_e32 v113, v205
	v_mov_b32_e32 v114, v206
	v_mov_b32_e32 v115, v207
	v_mov_b32_e32 v116, v208
	v_mov_b32_e32 v117, v209
	v_mov_b32_e32 v118, v210
	v_mov_b32_e32 v119, v211
	v_mov_b32_e32 v120, v212
	v_mov_b32_e32 v121, v213
	v_mov_b32_e32 v122, v214
	v_mov_b32_e32 v123, v215
	v_mov_b32_e32 v124, v216
	v_mov_b32_e32 v125, v217
	v_mov_b32_e32 v126, v218
	v_mov_b32_e32 v127, v219
	v_mov_b32_e32 v128, v220
	v_mov_b32_e32 v129, v221
	s_add_i32 s12, s12, 64
	s_cmpk_eq_i32 s12, 0x100
	s_cbranch_scc0 .LBB0_1110
	ds_write2_b32 v56, v26, v27 offset1:1
	ds_write2_b32 v56, v28, v29 offset0:2 offset1:3
	ds_write2_b32 v56, v22, v23 offset0:16 offset1:17
	ds_write2_b32 v56, v24, v25 offset0:18 offset1:19
	s_and_saveexec_b64 s[12:13], s[6:7]
	s_cbranch_execz .LBB0_1115
	ds_write_b32 v56, v14 offset:128
	s_or_b64 exec, exec, s[12:13]
	s_and_saveexec_b64 s[12:13], s[8:9]
	s_cbranch_execnz .LBB0_1116

; template <int MODE, bool OUTF32, bool HIN16 = false, bool HOUT16 = false>
; __device__ __forceinline__ void row_phase(LAS unsigned char* lds, const RowArgs& a, int G) {
;     ...
;         if (MODE == RM_ROUTE && tid < 32) cntl[tid] = 0;
;         f32x4 xs[RG];
;         if constexpr (MODE == RM_ROUTE && HIN16) {
;             const int fr = lane & 15, fq = lane >> 4;
;             f32x4 acc[2][3]; float sq[2] = {0.f, 0.f};
; #pragma unroll
;             for (int mt = 0; mt < 2; ++mt)
; #pragma unroll
;                 for (int nt = 0; nt < 3; ++nt) acc[mt][nt] = (f32x4){0.f, 0.f, 0.f, 0.f};
; #pragma unroll 2
;             for (int ks = 0; ks < 8; ++ks) { const int k0 = 256 * wave + 32 * ks + 8 * fq;
;                 bf16x8 af[2], bh[3], bl[3];
; #pragma unroll
;                 for (int mt = 0; mt < 2; ++mt) af[mt] = *(const bf16x8*)(a.hin16 + (size_t)(row0 + 16 * mt + fr) * D + k0);
; #pragma unroll
;                 for (int nt = 0; nt < 3; ++nt) { bh[nt] = *(const bf16x8*)(a.wr + (size_t)(16 * nt + fr) * D + k0); bl[nt] = *(const bf16x8*)(a.wr + (size_t)(48 + 16 * nt + fr) * D + k0); }
.LBB0_1942:
	s_and_saveexec_b64 s[14:15], s[4:5]
	ds_write_b32 v50, v5 offset:46208
	s_or_b64 exec, exec, s[14:15]
	s_lshl_b32 s63, s53, 5
	v_or_b32_e32 v2, s63, v51
	v_ashrrev_i32_e32 v3, 31, v2
	v_lshlrev_b64 v[42:43], 12, v[2:3]
	v_or_b32_e32 v2, 16, v2
	v_ashrrev_i32_e32 v3, 31, v2
	v_lshlrev_b64 v[44:45], 12, v[2:3]
	v_mov_b32_e32 v14, 0
	v_lshl_add_u64 v[46:47], s[36:37], 0, v[42:43]
	v_lshl_add_u64 v[48:49], s[36:37], 0, v[44:45]
	s_mov_b32 s14, 0
	v_mov_b32_e32 v15, v14
	v_mov_b32_e32 v16, v14
	v_mov_b32_e32 v17, v14
	v_mov_b32_e32 v22, v14
	v_mov_b32_e32 v23, v14
	v_mov_b32_e32 v24, v14
	v_mov_b32_e32 v25, v14
	v_mov_b32_e32 v26, v14
	v_mov_b32_e32 v27, v14
	v_mov_b32_e32 v28, v14
	v_mov_b32_e32 v29, v14
	v_mov_b32_e32 v10, v14
	v_mov_b32_e32 v11, v14
	v_mov_b32_e32 v12, v14
	v_mov_b32_e32 v13, v14
	v_mov_b32_e32 v18, v14
	v_mov_b32_e32 v19, v14
	v_mov_b32_e32 v20, v14
	v_mov_b32_e32 v21, v14
	v_mov_b32_e32 v6, v14
	v_mov_b32_e32 v7, v14
	v_mov_b32_e32 v8, v14
	v_mov_b32_e32 v9, v14
	v_mov_b32_e32 v2, v14
	v_mov_b32_e32 v3, v14
	s_mov_b32 s98, 0
	v_add_u32_e32 v158, s98, v60
	v_ashrrev_i32_e32 v159, 31, v158
	v_add_u32_e32 v160, 32, v158
	v_lshlrev_b64 v[158:159], 1, v[158:159]
	v_lshl_add_u64 v[162:163], s[36:37], 0, v[158:159]
	v_lshl_add_u64 v[158:159], s[46:47], 0, v[158:159]
	v_lshl_add_u64 v[174:175], v[158:159], 0, v[36:37]
	v_add_co_u32_e32 v194, vcc, s54, v174
	v_ashrrev_i32_e32 v161, 31, v160
	s_nop 0
	v_addc_co_u32_e32 v195, vcc, 0, v175, vcc
	v_add_co_u32_e32 v198, vcc, s55, v174
	v_lshlrev_b64 v[160:161], 1, v[160:161]
	s_nop 0
	v_addc_co_u32_e32 v199, vcc, 0, v175, vcc
	v_add_co_u32_e32 v192, vcc, s56, v174
	v_lshl_add_u64 v[164:165], v[162:163], 0, v[42:43]
	v_lshl_add_u64 v[162:163], v[162:163], 0, v[44:45]
	v_addc_co_u32_e32 v193, vcc, 0, v175, vcc
	v_lshl_add_u64 v[170:171], v[158:159], 0, v[38:39]
	v_lshl_add_u64 v[176:177], v[46:47], 0, v[160:161]
	v_lshl_add_u64 v[178:179], v[48:49], 0, v[160:161]
	v_lshl_add_u64 v[190:191], v[32:33], 0, v[160:161]
	v_lshl_add_u64 v[186:187], v[34:35], 0, v[160:161]
	global_load_dwordx4 v[158:161], v[164:165], off
	s_nop 0
	global_load_dwordx4 v[162:165], v[162:163], off
	s_nop 0
	global_load_dwordx4 v[166:169], v[174:175], off
	v_add_co_u32_e32 v202, vcc, s57, v174
	global_load_dwordx4 v[170:173], v[170:171], off
	s_nop 0
	v_addc_co_u32_e32 v203, vcc, 0, v175, vcc
	v_add_co_u32_e32 v210, vcc, s54, v190
	global_load_dwordx4 v[174:177], v[176:177], off
	s_nop 0
	global_load_dwordx4 v[178:181], v[178:179], off
	s_nop 0
	global_load_dwordx4 v[182:185], v[190:191], off
	v_addc_co_u32_e32 v211, vcc, 0, v191, vcc
	v_add_co_u32_e32 v214, vcc, s55, v190
	global_load_dwordx4 v[186:189], v[186:187], off
	s_nop 0
	v_addc_co_u32_e32 v215, vcc, 0, v191, vcc
	v_add_co_u32_e32 v206, vcc, s56, v190
	s_nop 0
	s_nop 0
	v_addc_co_u32_e32 v207, vcc, 0, v191, vcc
	v_add_co_u32_e32 v218, vcc, s57, v190
	s_nop 0
	s_nop 0
	v_addc_co_u32_e32 v219, vcc, 0, v191, vcc
	global_load_dwordx4 v[190:193], v[192:193], off
	s_nop 0
	global_load_dwordx4 v[194:197], v[194:195], off
	s_nop 0
	global_load_dwordx4 v[198:201], v[198:199], off
	s_nop 0
	global_load_dwordx4 v[202:205], v[202:203], off
	s_nop 0
	global_load_dwordx4 v[206:209], v[206:207], off
	s_nop 0
	global_load_dwordx4 v[210:213], v[210:211], off
	s_nop 0
	global_load_dwordx4 v[214:217], v[214:215], off
	s_nop 0
	global_load_dwordx4 v[218:221], v[218:219], off
	s_waitcnt vmcnt(0)
	v_mov_b32_e32 v66, v158
	v_mov_b32_e32 v67, v159
	v_mov_b32_e32 v68, v160
	v_mov_b32_e32 v69, v161
	v_mov_b32_e32 v70, v162
	v_mov_b32_e32 v71, v163
	v_mov_b32_e32 v72, v164
	v_mov_b32_e32 v73, v165
	v_mov_b32_e32 v74, v166
	v_mov_b32_e32 v75, v167
	v_mov_b32_e32 v76, v168
	v_mov_b32_e32 v77, v169
	v_mov_b32_e32 v78, v170
	v_mov_b32_e32 v79, v171
	v_mov_b32_e32 v80, v172
	v_mov_b32_e32 v81, v173
	v_mov_b32_e32 v82, v174
	v_mov_b32_e32 v83, v175
	v_mov_b32_e32 v84, v176
	v_mov_b32_e32 v85, v177
	v_mov_b32_e32 v86, v178
	v_mov_b32_e32 v87, v179
	v_mov_b32_e32 v88, v180
	v_mov_b32_e32 v89, v181
	v_mov_b32_e32 v90, v182
	v_mov_b32_e32 v91, v183
	v_mov_b32_e32 v92, v184
	v_mov_b32_e32 v93, v185
	v_mov_b32_e32 v94, v186
	v_mov_b32_e32 v95, v187
	v_mov_b32_e32 v96, v188
	v_mov_b32_e32 v97, v189
	v_mov_b32_e32 v98, v190
	v_mov_b32_e32 v99, v191
	v_mov_b32_e32 v100, v192
	v_mov_b32_e32 v101, v193
	v_mov_b32_e32 v102, v194
	v_mov_b32_e32 v103, v195
	v_mov_b32_e32 v104, v196
	v_mov_b32_e32 v105, v197
	v_mov_b32_e32 v106, v198
	v_mov_b32_e32 v107, v199
	v_mov_b32_e32 v108, v200
	v_mov_b32_e32 v109, v201
	v_mov_b32_e32 v110, v202
	v_mov_b32_e32 v111, v203
	v_mov_b32_e32 v112, v204
	v_mov_b32_e32 v113, v205
	v_mov_b32_e32 v114, v206
	v_mov_b32_e32 v115, v207
	v_mov_b32_e32 v116, v208
	v_mov_b32_e32 v117, v209
	v_mov_b32_e32 v118, v210
	v_mov_b32_e32 v119, v211
	v_mov_b32_e32 v120, v212
	v_mov_b32_e32 v121, v213
	v_mov_b32_e32 v122, v214
	v_mov_b32_e32 v123, v215
	v_mov_b32_e32 v124, v216
	v_mov_b32_e32 v125, v217
	v_mov_b32_e32 v126, v218
	v_mov_b32_e32 v127, v219
	v_mov_b32_e32 v128, v220
	v_mov_b32_e32 v129, v221
; #define MFMA16(b, a, c) __builtin_amdgcn_mfma_f32_16x16x32_bf16((b), (a), (c), 0, 0, 0)
; template <int MODE, bool OUTF32, bool HIN16 = false, bool HOUT16 = false>
; __device__ __forceinline__ void row_phase(LAS unsigned char* lds, const RowArgs& a, int G) {
;     ...
;             for (int ks = 0; ks < 8; ++ks) { const int k0 = 256 * wave + 32 * ks + 8 * fq;
;                 bf16x8 af[2], bh[3], bl[3];
; #pragma unroll
;                 for (int mt = 0; mt < 2; ++mt) af[mt] = *(const bf16x8*)(a.hin16 + (size_t)(row0 + 16 * mt + fr) * D + k0);
; #pragma unroll
;                 for (int nt = 0; nt < 3; ++nt) { bh[nt] = *(const bf16x8*)(a.wr + (size_t)(16 * nt + fr) * D + k0); bl[nt] = *(const bf16x8*)(a.wr + (size_t)(48 + 16 * nt + fr) * D + k0); }
; #pragma unroll
;                 for (int mt = 0; mt < 2; ++mt) {
; #pragma unroll
;                     for (int e = 0; e < 8; ++e) { const float v = bf2f((unsigned short)af[mt][e]); sq[mt] += v * v; }
; #pragma unroll
;                     for (int nt = 0; nt < 3; ++nt) { acc[mt][nt] = MFMA16(bh[nt], af[mt], acc[mt][nt]); acc[mt][nt] = MFMA16(bl[nt], af[mt], acc[mt][nt]); } }
.LBB0_1945:
	s_add_i32 s98, s14, 64
	s_min_u32 s98, s98, 0xc0
	v_add_u32_e32 v158, s98, v60
	v_ashrrev_i32_e32 v159, 31, v158
	v_add_u32_e32 v160, 32, v158
	v_lshlrev_b64 v[158:159], 1, v[158:159]
	v_lshl_add_u64 v[162:163], s[36:37], 0, v[158:159]
	v_lshl_add_u64 v[158:159], s[46:47], 0, v[158:159]
	v_lshl_add_u64 v[174:175], v[158:159], 0, v[36:37]
	v_add_co_u32_e32 v194, vcc, s54, v174
	v_ashrrev_i32_e32 v161, 31, v160
	s_nop 0
	v_addc_co_u32_e32 v195, vcc, 0, v175, vcc
	v_add_co_u32_e32 v198, vcc, s55, v174
	v_lshlrev_b64 v[160:161], 1, v[160:161]
	s_nop 0
	v_addc_co_u32_e32 v199, vcc, 0, v175, vcc
	v_add_co_u32_e32 v192, vcc, s56, v174
	v_lshl_add_u64 v[164:165], v[162:163], 0, v[42:43]
	v_lshl_add_u64 v[162:163], v[162:163], 0, v[44:45]
	v_addc_co_u32_e32 v193, vcc, 0, v175, vcc
	v_lshl_add_u64 v[170:171], v[158:159], 0, v[38:39]
	v_lshl_add_u64 v[176:177], v[46:47], 0, v[160:161]
	v_lshl_add_u64 v[178:179], v[48:49], 0, v[160:161]
	v_lshl_add_u64 v[190:191], v[32:33], 0, v[160:161]
	v_lshl_add_u64 v[186:187], v[34:35], 0, v[160:161]
	global_load_dwordx4 v[158:161], v[164:165], off
	s_nop 0
	global_load_dwordx4 v[162:165], v[162:163], off
	s_nop 0
	global_load_dwordx4 v[166:169], v[174:175], off
	v_add_co_u32_e32 v202, vcc, s57, v174
	global_load_dwordx4 v[170:173], v[170:171], off
	s_nop 0
	v_addc_co_u32_e32 v203, vcc, 0, v175, vcc
	v_add_co_u32_e32 v210, vcc, s54, v190
	global_load_dwordx4 v[174:177], v[176:177], off
	s_nop 0
	global_load_dwordx4 v[178:181], v[178:179], off
	s_nop 0
	global_load_dwordx4 v[182:185], v[190:191], off
	v_addc_co_u32_e32 v211, vcc, 0, v191, vcc
	v_add_co_u32_e32 v214, vcc, s55, v190
	global_load_dwordx4 v[186:189], v[186:187], off
	s_nop 0
	v_addc_co_u32_e32 v215, vcc, 0, v191, vcc
	v_add_co_u32_e32 v206, vcc, s56, v190
	s_nop 0
	s_nop 0
	v_addc_co_u32_e32 v207, vcc, 0, v191, vcc
	v_add_co_u32_e32 v218, vcc, s57, v190
	s_nop 0
	s_nop 0
	v_addc_co_u32_e32 v219, vcc, 0, v191, vcc
	global_load_dwordx4 v[190:193], v[192:193], off
	s_nop 0
	global_load_dwordx4 v[194:197], v[194:195], off
	s_nop 0
	global_load_dwordx4 v[198:201], v[198:199], off
	s_nop 0
	global_load_dwordx4 v[202:205], v[202:203], off
	s_nop 0
	global_load_dwordx4 v[206:209], v[206:207], off
	s_nop 0
	global_load_dwordx4 v[210:213], v[210:211], off
	s_nop 0
	global_load_dwordx4 v[214:217], v[214:215], off
	s_nop 0
	global_load_dwordx4 v[218:221], v[218:219], off
	v_mfma_f32_16x16x32_bf16 v[26:29], v[74:77], v[66:69], v[26:29]
	v_and_b32_e32 v131, 0xffff0000, v70
	v_lshlrev_b32_e32 v130, 16, v70
	v_lshlrev_b32_e32 v4, 16, v66
	v_mfma_f32_16x16x32_bf16 v[10:13], v[74:77], v[70:73], v[10:13]
	v_and_b32_e32 v40, 0xffff0000, v66
	v_and_b32_e32 v133, 0xffff0000, v71
	v_lshlrev_b32_e32 v132, 16, v71
	v_mfma_f32_16x16x32_bf16 v[26:29], v[102:105], v[66:69], v[26:29]
	v_lshlrev_b32_e32 v65, 16, v67
	v_and_b32_e32 v139, 0xffff0000, v67
	v_lshlrev_b32_e32 v141, 16, v68
	v_mfma_f32_16x16x32_bf16 v[10:13], v[102:105], v[70:73], v[10:13]
	v_mul_f32_e64 v102, v130, v130
	v_mul_f32_e64 v103, v131, v131
	v_pk_mul_f32 v[104:105], v[132:133], v[132:133]
	v_and_b32_e32 v135, 0xffff0000, v72
	v_mfma_f32_16x16x32_bf16 v[14:17], v[98:101], v[66:69], v[14:17]
	v_lshlrev_b32_e32 v134, 16, v72
	v_mul_f32_e32 v138, v65, v65
	v_mul_f32_e32 v140, v139, v139
	v_mfma_f32_16x16x32_bf16 v[6:9], v[98:101], v[70:73], v[6:9]
	v_mul_f32_e32 v98, v4, v4
	v_mov_b32_e32 v99, v102
	v_mul_f32_e32 v100, v40, v40
	v_mfma_f32_16x16x32_bf16 v[22:25], v[78:81], v[66:69], v[22:25]
	v_mov_b32_e32 v101, v103
	v_pk_add_f32 v[2:3], v[2:3], v[98:99]
	v_mov_b32_e32 v139, v104
	v_mfma_f32_16x16x32_bf16 v[18:21], v[78:81], v[70:73], v[18:21]
	v_add_f32_e64 v2, v100, v2
	v_add_f32_e64 v3, v101, v3
	v_and_b32_e32 v143, 0xffff0000, v68
	v_mul_f32_e32 v142, v141, v141
	v_pk_mul_f32 v[130:131], v[134:135], v[134:135]
	v_mov_b32_e32 v141, v105
	v_pk_add_f32 v[2:3], v[138:139], v[2:3]
	v_lshlrev_b32_e32 v145, 16, v69
	v_and_b32_e32 v137, 0xffff0000, v73
	v_lshlrev_b32_e32 v136, 16, v73
	v_mul_f32_e32 v144, v143, v143
	v_mov_b32_e32 v143, v130
	v_pk_add_f32 v[2:3], v[140:141], v[2:3]
	v_and_b32_e32 v147, 0xffff0000, v69
	v_mfma_f32_16x16x32_bf16 v[22:25], v[106:109], v[66:69], v[22:25]
	v_mul_f32_e32 v146, v145, v145
	v_mov_b32_e32 v145, v131
	v_pk_add_f32 v[2:3], v[142:143], v[2:3]
	v_mfma_f32_16x16x32_bf16 v[18:21], v[106:109], v[70:73], v[18:21]
	v_mul_f32_e64 v106, v136, v136
	v_mul_f32_e64 v107, v137, v137
	v_lshlrev_b32_e32 v149, 16, v82
	v_and_b32_e32 v75, 0xffff0000, v86
	v_mfma_f32_16x16x32_bf16 v[14:17], v[110:113], v[66:69], v[14:17]
	v_lshlrev_b32_e32 v74, 16, v86
; #define MFMA16(b, a, c) __builtin_amdgcn_mfma_f32_16x16x32_bf16((b), (a), (c), 0, 0, 0)
; template <int MODE, bool OUTF32, bool HIN16 = false, bool HOUT16 = false>
; __device__ __forceinline__ void row_phase(LAS unsigned char* lds, const RowArgs& a, int G) {
;     ...
;                 for (int mt = 0; mt < 2; ++mt) {
; #pragma unroll
;                     for (int e = 0; e < 8; ++e) { const float v = bf2f((unsigned short)af[mt][e]); sq[mt] += v * v; }
; #pragma unroll
;                     for (int nt = 0; nt < 3; ++nt) { acc[mt][nt] = MFMA16(bh[nt], af[mt], acc[mt][nt]); acc[mt][nt] = MFMA16(bl[nt], af[mt], acc[mt][nt]); } }
;             }
; #pragma unroll
;             for (int mt = 0; mt < 2; ++mt) { const int r = 16 * mt + fr;
; #pragma unroll
;                 for (int nt = 0; nt < 3; ++nt)
; #pragma unroll
;                     for (int i = 0; i < 4; ++i) { const int o = 16 * nt + 4 * fq + i; if (o < 36) red[(r * 8 + wave) * NRED + o] = acc[mt][nt][i]; }
;                 float s = sq[mt]; s += __shfl_xor(s, 16); s += __shfl_xor(s, 32);
;                 if (fq == 0) red[(r * 8 + wave) * NRED + 36] = s; }
	v_mul_f32_e32 v148, v147, v147
	v_mov_b32_e32 v147, v106
	v_mfma_f32_16x16x32_bf16 v[6:9], v[110:113], v[70:73], v[6:9]
	v_add_f32_e64 v2, v144, v2
	v_add_f32_e64 v3, v145, v3
	v_mul_f32_e32 v108, v149, v149
	v_pk_mul_f32 v[74:75], v[74:75], v[74:75]
	v_mov_b32_e32 v149, v107
	v_pk_add_f32 v[2:3], v[146:147], v[2:3]
	v_and_b32_e32 v150, 0xffff0000, v82
	v_and_b32_e32 v77, 0xffff0000, v87
	v_lshlrev_b32_e32 v76, 16, v87
	v_mov_b32_e32 v109, v74
	v_pk_add_f32 v[2:3], v[148:149], v[2:3]
	v_lshlrev_b32_e32 v151, 16, v83
	v_mul_f32_e32 v132, v150, v150
	v_mfma_f32_16x16x32_bf16 v[26:29], v[90:93], v[82:85], v[26:29]
	v_mul_f32_e64 v76, v76, v76
	v_mul_f32_e64 v77, v77, v77
	v_mov_b32_e32 v133, v75
	v_pk_add_f32 v[2:3], v[2:3], v[108:109]
	v_mfma_f32_16x16x32_bf16 v[22:25], v[94:97], v[82:85], v[22:25]
	v_and_b32_e32 v152, 0xffff0000, v83
	v_and_b32_e32 v79, 0xffff0000, v88
	v_lshlrev_b32_e32 v78, 16, v88
	v_mfma_f32_16x16x32_bf16 v[10:13], v[90:93], v[86:89], v[10:13]
	v_mul_f32_e32 v66, v151, v151
	v_mov_b32_e32 v67, v76
	v_pk_add_f32 v[2:3], v[132:133], v[2:3]
	v_mfma_f32_16x16x32_bf16 v[18:21], v[94:97], v[86:89], v[18:21]
	v_lshlrev_b32_e32 v153, 16, v84
	v_mul_f32_e32 v68, v152, v152
	v_pk_mul_f32 v[78:79], v[78:79], v[78:79]
	v_mfma_f32_16x16x32_bf16 v[14:17], v[114:117], v[82:85], v[14:17]
	v_mov_b32_e32 v69, v77
	v_pk_add_f32 v[2:3], v[66:67], v[2:3]
	v_and_b32_e32 v154, 0xffff0000, v84
	v_mfma_f32_16x16x32_bf16 v[6:9], v[114:117], v[86:89], v[6:9]
	v_and_b32_e32 v81, 0xffff0000, v89
	v_lshlrev_b32_e32 v80, 16, v89
	v_mul_f32_e32 v134, v153, v153
	v_mov_b32_e32 v135, v78
	v_pk_add_f32 v[2:3], v[68:69], v[2:3]
	v_lshlrev_b32_e32 v155, 16, v85
	v_mul_f32_e32 v70, v154, v154
	v_pk_mul_f32 v[80:81], v[80:81], v[80:81]
	v_mov_b32_e32 v71, v79
	v_mfma_f32_16x16x32_bf16 v[26:29], v[118:121], v[82:85], v[26:29]
	v_add_f32_e64 v2, v134, v2
	v_add_f32_e64 v3, v135, v3
	v_and_b32_e32 v156, 0xffff0000, v85
	v_mul_f32_e32 v72, v155, v155
	v_mfma_f32_16x16x32_bf16 v[22:25], v[122:125], v[82:85], v[22:25]
	v_mov_b32_e32 v73, v80
	v_pk_add_f32 v[2:3], v[70:71], v[2:3]
	v_mul_f32_e32 v110, v156, v156
	v_mfma_f32_16x16x32_bf16 v[10:13], v[118:121], v[86:89], v[10:13]
	v_mov_b32_e32 v111, v81
	v_pk_add_f32 v[2:3], v[72:73], v[2:3]
	v_mfma_f32_16x16x32_bf16 v[18:21], v[122:125], v[86:89], v[18:21]
	v_add_f32_e64 v2, v110, v2
	v_add_f32_e64 v3, v111, v3
	v_mfma_f32_16x16x32_bf16 v[14:17], v[126:129], v[82:85], v[14:17]
	v_mfma_f32_16x16x32_bf16 v[6:9], v[126:129], v[86:89], v[6:9]
	s_waitcnt vmcnt(0)
	v_mov_b32_e32 v66, v158
	v_mov_b32_e32 v67, v159
	v_mov_b32_e32 v68, v160
	v_mov_b32_e32 v69, v161
	v_mov_b32_e32 v70, v162
	v_mov_b32_e32 v71, v163
	v_mov_b32_e32 v72, v164
	v_mov_b32_e32 v73, v165
	v_mov_b32_e32 v74, v166
	v_mov_b32_e32 v75, v167
	v_mov_b32_e32 v76, v168
	v_mov_b32_e32 v77, v169
	v_mov_b32_e32 v78, v170
	v_mov_b32_e32 v79, v171
	v_mov_b32_e32 v80, v172
	v_mov_b32_e32 v81, v173
	v_mov_b32_e32 v82, v174
	v_mov_b32_e32 v83, v175
	v_mov_b32_e32 v84, v176
	v_mov_b32_e32 v85, v177
	v_mov_b32_e32 v86, v178
	v_mov_b32_e32 v87, v179
	v_mov_b32_e32 v88, v180
	v_mov_b32_e32 v89, v181
	v_mov_b32_e32 v90, v182
	v_mov_b32_e32 v91, v183
	v_mov_b32_e32 v92, v184
	v_mov_b32_e32 v93, v185
	v_mov_b32_e32 v94, v186
	v_mov_b32_e32 v95, v187
	v_mov_b32_e32 v96, v188
	v_mov_b32_e32 v97, v189
	v_mov_b32_e32 v98, v190
	v_mov_b32_e32 v99, v191
	v_mov_b32_e32 v100, v192
	v_mov_b32_e32 v101, v193
	v_mov_b32_e32 v102, v194
	v_mov_b32_e32 v103, v195
	v_mov_b32_e32 v104, v196
	v_mov_b32_e32 v105, v197
	v_mov_b32_e32 v106, v198
	v_mov_b32_e32 v107, v199
	v_mov_b32_e32 v108, v200
	v_mov_b32_e32 v109, v201
	v_mov_b32_e32 v110, v202
	v_mov_b32_e32 v111, v203
	v_mov_b32_e32 v112, v204
	v_mov_b32_e32 v113, v205
	v_mov_b32_e32 v114, v206
	v_mov_b32_e32 v115, v207
	v_mov_b32_e32 v116, v208
	v_mov_b32_e32 v117, v209
	v_mov_b32_e32 v118, v210
	v_mov_b32_e32 v119, v211
	v_mov_b32_e32 v120, v212
	v_mov_b32_e32 v121, v213
	v_mov_b32_e32 v122, v214
	v_mov_b32_e32 v123, v215
	v_mov_b32_e32 v124, v216
	v_mov_b32_e32 v125, v217
	v_mov_b32_e32 v126, v218
	v_mov_b32_e32 v127, v219
	v_mov_b32_e32 v128, v220
	v_mov_b32_e32 v129, v221
	s_add_i32 s14, s14, 64
	s_cmpk_eq_i32 s14, 0x100
	s_cbranch_scc0 .LBB0_1945
	ds_write2_b32 v56, v26, v27 offset1:1
	ds_write2_b32 v56, v28, v29 offset0:2 offset1:3
	ds_write2_b32 v56, v22, v23 offset0:16 offset1:17
	ds_write2_b32 v56, v24, v25 offset0:18 offset1:19
	s_and_saveexec_b64 s[14:15], s[8:9]
	s_cbranch_execz .LBB0_1950
	ds_write_b32 v56, v14 offset:128
	s_or_b64 exec, exec, s[14:15]
	s_and_saveexec_b64 s[14:15], s[10:11]
	s_cbranch_execnz .LBB0_1951

; __global__ void __launch_bounds__(NTHR, 2) mk_fwd(Args args) {
	.amdhsa_kernel _Z6mk_fwd4Args
		.amdhsa_group_segment_fixed_size 0
		.amdhsa_private_segment_fixed_size 0
		.amdhsa_kernarg_size 504
		.amdhsa_user_sgpr_count 2
		.amdhsa_user_sgpr_dispatch_ptr 0
		.amdhsa_user_sgpr_queue_ptr 0
		.amdhsa_user_sgpr_kernarg_segment_ptr 1
		.amdhsa_user_sgpr_dispatch_id 0
		.amdhsa_user_sgpr_kernarg_preload_length 0
		.amdhsa_user_sgpr_kernarg_preload_offset 0
		.amdhsa_user_sgpr_private_segment_size 0
		.amdhsa_uses_dynamic_stack 0
		.amdhsa_enable_private_segment 0
		.amdhsa_system_sgpr_workgroup_id_x 1
		.amdhsa_system_sgpr_workgroup_id_y 0
		.amdhsa_system_sgpr_workgroup_id_z 0
		.amdhsa_system_sgpr_workgroup_info 0
		.amdhsa_system_vgpr_workitem_id 0
		.amdhsa_next_free_vgpr 251
		.amdhsa_next_free_sgpr 100
		.amdhsa_accum_offset 252
		.amdhsa_reserve_vcc 1
		.amdhsa_float_round_mode_32 0
		.amdhsa_float_round_mode_16_64 0
		.amdhsa_float_denorm_mode_32 3
		.amdhsa_float_denorm_mode_16_64 3
		.amdhsa_dx10_clamp 1
		.amdhsa_ieee_mode 1
		.amdhsa_fp16_overflow 0
		.amdhsa_tg_split 0
		.amdhsa_exception_fp_ieee_invalid_op 0
		.amdhsa_exception_fp_denorm_src 0
		.amdhsa_exception_fp_ieee_div_zero 0
		.amdhsa_exception_fp_ieee_overflow 0
		.amdhsa_exception_fp_ieee_underflow 0
		.amdhsa_exception_fp_ieee_inexact 0
		.amdhsa_exception_int_div_zero 0
	.end_amdhsa_kernel

; __global__ void __launch_bounds__(NTHR, 2) mk_fwd(Args args) {
amdhsa.kernels:
  - .agpr_count:     0
    .args:
      - .offset:         0
        .size:           248
        .value_kind:     by_value
      - .offset:         248
        .size:           4
        .value_kind:     hidden_block_count_x
      - .offset:         252
        .size:           4
        .value_kind:     hidden_block_count_y
      - .offset:         256
        .size:           4
        .value_kind:     hidden_block_count_z
      - .offset:         260
        .size:           2
        .value_kind:     hidden_group_size_x
      - .offset:         262
        .size:           2
        .value_kind:     hidden_group_size_y
      - .offset:         264
        .size:           2
        .value_kind:     hidden_group_size_z
      - .offset:         266
        .size:           2
        .value_kind:     hidden_remainder_x
      - .offset:         268
        .size:           2
        .value_kind:     hidden_remainder_y
      - .offset:         270
        .size:           2
        .value_kind:     hidden_remainder_z
      - .offset:         288
        .size:           8
        .value_kind:     hidden_global_offset_x
      - .offset:         296
        .size:           8
        .value_kind:     hidden_global_offset_y
      - .offset:         304
        .size:           8
        .value_kind:     hidden_global_offset_z
      - .offset:         312
        .size:           2
        .value_kind:     hidden_grid_dims
      - .offset:         368
        .size:           4
        .value_kind:     hidden_dynamic_lds_size
    .group_segment_fixed_size: 0
    .kernarg_segment_align: 8
    .kernarg_segment_size: 504
    .language:       OpenCL C
    .language_version:
      - 2
      - 0
    .max_flat_workgroup_size: 512
    .name:           _Z6mk_fwd4Args
    .private_segment_fixed_size: 0
    .sgpr_count:     106
    .sgpr_spill_count: 6
    .symbol:         _Z6mk_fwd4Args.kd
    .uniform_work_group_size: 1
    .uses_dynamic_stack: false
    .vgpr_count:     251
    .vgpr_spill_count: 0
    .wavefront_size: 64
